# v23 + combination: GEMM1 XCD stagger 2.4 us, HGRN2 chunk-loop instruction selection, HGRN2 header counted waits
# speedup vs baseline: 1.0069x; 1.0013x over previous
.LBB0_354:
	v_add_u32_e32 v8, 0x200, v8
	s_movk_i32 s70, 0x1fff
	v_cmp_lt_u32_e32 vcc, s70, v8
	ds_write_b32 v7, v69
	s_or_b64 s[58:59], vcc, s[58:59]
	v_add_u32_e32 v7, 0x800, v7
	s_andn2_b64 exec, exec, s[58:59]
	s_cbranch_execnz .LBB0_354
	s_or_b64 exec, exec, s[58:59]
	s_waitcnt vmcnt(0)
	v_sub_f32_e32 v4, v4, v2
	v_mul_f32_e32 v2, 0x3fb8aa3b, v4
	s_mov_b32 s46, 0x3fb8aa3b
	v_fma_f32 v7, v4, s46, -v2
	v_rndne_f32_e32 v8, v2
	v_fmac_f32_e32 v7, 0x32a5705f, v4
	v_sub_f32_e32 v2, v2, v8
	v_add_f32_e32 v2, v2, v7
	v_cvt_i32_f32_e32 v7, v8
	v_exp_f32_e32 v2, v2
	v_sub_f32_e32 v3, v5, v3
	s_and_b64 s[58:59], s[40:41], exec
	v_readlane_b32 s58, v254, 15
	v_ldexp_f32 v7, v2, v7
	v_mul_f32_e32 v2, 0x3fb8aa3b, v3
	v_fma_f32 v5, v3, s46, -v2
	v_rndne_f32_e32 v8, v2
	v_fmac_f32_e32 v5, 0x32a5705f, v3
	v_sub_f32_e32 v2, v2, v8
	v_add_f32_e32 v2, v2, v5
	v_exp_f32_e32 v5, v2
	v_cvt_i32_f32_e32 v8, v8
	s_mov_b32 s46, 0xc2ce8ed0
	v_cmp_ngt_f32_e32 vcc, s46, v4
	s_mov_b32 s89, 0x42b17218
	v_ldexp_f32 v5, v5, v8
	v_cndmask_b32_e32 v7, 0, v7, vcc
	v_cmp_ngt_f32_e32 vcc, s46, v3
	v_readlane_b32 s46, v254, 26
	s_cselect_b32 s58, s58, s46
	v_cndmask_b32_e32 v5, 0, v5, vcc
	v_cmp_nlt_f32_e32 vcc, s89, v3
	s_mulk_i32 s58, 0x1c00
	v_readlane_b32 s46, v254, 27
	v_cndmask_b32_e32 v3, v215, v5, vcc
	v_or_b32_e32 v5, s58, v6
	s_cselect_b32 s58, s60, s46
	s_mulk_i32 s58, 0x1c00
	v_readlane_b32 s46, v254, 28
	v_readlane_b32 s47, v254, 29
	v_or_b32_e32 v8, s58, v6
	s_cselect_b32 s58, s46, s47
	s_mulk_i32 s58, 0x1c00
	v_readlane_b32 s46, v254, 30
	v_readlane_b32 s47, v254, 31
	v_or_b32_e32 v9, s58, v6
	s_cselect_b32 s58, s46, s47
	s_mulk_i32 s58, 0x1c00
	v_readlane_b32 s46, v254, 32
	v_readlane_b32 s47, v254, 33
	v_or_b32_e32 v10, s58, v6
	s_cselect_b32 s58, s46, s47
	s_mulk_i32 s58, 0x1c00
	v_readlane_b32 s46, v254, 34
	v_readlane_b32 s47, v254, 35
	v_or_b32_e32 v11, s58, v6
	s_cselect_b32 s58, s46, s47
	s_mulk_i32 s58, 0x1c00
	v_readlane_b32 s46, v254, 36
	v_readlane_b32 s47, v254, 37
	v_or_b32_e32 v12, s58, v6
	s_cselect_b32 s58, s46, s47
	s_mulk_i32 s58, 0x1c00
	v_readlane_b32 s46, v254, 38
	v_readlane_b32 s47, v254, 39
	v_or_b32_e32 v13, s58, v6
	s_cselect_b32 s58, s46, s47
	s_mulk_i32 s58, 0x1c00
	v_add_f32_e32 v3, 1.0, v3
	v_or_b32_e32 v6, s58, v6
	v_lshlrev_b32_e32 v50, 1, v6
	v_div_scale_f32 v6, s[58:59], v3, v3, 1.0
	s_movk_i32 s58, 0x1800
	s_cselect_b32 s70, s58, 0x2000
	s_mov_b32 s58, 0x16600000
	s_cselect_b32 s58, s58, 0x1a600000
	s_add_u32 s82, s66, s58
	s_addc_u32 s83, s67, 0
	s_lshl_b32 s58, s5, 7
	s_and_b32 s88, s58, 0xfffff800
	s_and_b64 s[58:59], s[40:41], exec
	s_cselect_b32 s58, 0, 0x7c0
	s_or_b32 s58, s58, s88
	s_mul_hi_i32 s59, s58, 0x3800
	s_mulk_i32 s58, 0x3800
	s_add_u32 s86, s55, s58
	s_addc_u32 s87, s73, s59
	s_add_u32 s58, s86, s70
	s_addc_u32 s59, s87, 0
	s_add_u32 s84, s86, 0x1000
	s_addc_u32 s85, s87, 0
	v_lshlrev_b32_e32 v68, 1, v5
	s_add_u32 s86, s86, 0x2800
	v_lshlrev_b32_e32 v52, 1, v8
	v_lshlrev_b32_e32 v54, 1, v9
	v_lshlrev_b32_e32 v56, 1, v10
	v_lshlrev_b32_e32 v58, 1, v11
	v_lshlrev_b32_e32 v60, 1, v12
	v_lshlrev_b32_e32 v62, 1, v13
	s_addc_u32 s87, s87, 0
	global_load_dword v87, v68, s[58:59]
	global_load_dword v89, v68, s[84:85]
	global_load_dword v91, v68, s[86:87]
	global_load_dword v93, v52, s[58:59]
	global_load_dword v97, v52, s[84:85]
	global_load_dword v107, v52, s[86:87]
	global_load_dword v147, v54, s[84:85]
	global_load_dword v148, v54, s[86:87]
	global_load_dword v146, v54, s[58:59]
	global_load_dword v149, v56, s[58:59]
	global_load_dword v150, v56, s[84:85]
	global_load_dword v151, v56, s[86:87]
	global_load_dword v152, v58, s[58:59]
	global_load_dword v153, v58, s[84:85]
	global_load_dword v154, v58, s[86:87]
	global_load_dword v157, v60, s[86:87]
	global_load_dword v155, v60, s[58:59]
	global_load_dword v156, v60, s[84:85]
	global_load_dword v158, v62, s[58:59]
	global_load_dword v159, v62, s[84:85]
	global_load_dword v160, v62, s[86:87]
	global_load_dword v161, v50, s[58:59]
	global_load_dword v164, v50, s[84:85]
	global_load_dword v165, v50, s[86:87]
	global_load_dword v70, v50, s[86:87]
	global_load_dword v70, v50, s[86:87]
	global_load_dword v70, v50, s[86:87]
	global_load_dword v70, v50, s[86:87]
	v_rcp_f32_e32 v14, v6
	v_cmp_nlt_f32_e32 vcc, s89, v4
	v_readlane_b32 s46, v254, 40
	s_waitcnt lgkmcnt(0)
	v_fma_f32 v5, -v6, v14, 1.0
	v_cndmask_b32_e32 v4, v215, v7, vcc
	v_fmac_f32_e32 v14, v5, v14
	v_div_scale_f32 v5, vcc, 1.0, v3, 1.0
	v_mul_f32_e32 v7, v5, v14
	v_fma_f32 v8, -v6, v7, v5
	v_fmac_f32_e32 v7, v8, v14
	v_fma_f32 v5, -v6, v7, v5
	v_add_f32_e32 v4, 1.0, v4
	v_div_fmas_f32 v5, v5, v14, v7
	v_div_fixup_f32 v65, v5, v3, 1.0
	v_div_scale_f32 v3, s[58:59], v4, v4, 1.0
	v_rcp_f32_e32 v5, v3
	v_or_b32_e32 v6, s61, v189
	v_lshlrev_b32_e32 v6, 1, v6
	s_barrier
	v_fma_f32 v7, -v3, v5, 1.0
	v_fmac_f32_e32 v5, v7, v5
	v_div_scale_f32 v7, vcc, 1.0, v4, 1.0
	v_mul_f32_e32 v8, v7, v5
	v_fma_f32 v9, -v3, v8, v7
	v_fmac_f32_e32 v8, v9, v5
	v_fma_f32 v3, -v3, v8, v7
	v_div_fmas_f32 v3, v3, v5, v8
	v_div_fixup_f32 v64, v3, v4, 1.0
	v_cndmask_b32_e64 v3, v188, v187, s[40:41]
	v_lshlrev_b32_e32 v3, 11, v3
	v_mov_b32_e32 v2, 0
	v_or3_b32 v4, v6, s46, v3
	v_mov_b32_e32 v5, v69
	s_mov_b32 s89, 0
	v_pk_add_f32 v[108:109], v[64:65], 1.0 op_sel_hi:[1,0] neg_lo:[1,0] neg_hi:[1,0]
	v_mov_b32_e32 v53, v69
	v_mov_b32_e32 v55, v69
	v_mov_b32_e32 v57, v69
	v_mov_b32_e32 v59, v69
	v_mov_b32_e32 v61, v69
	v_mov_b32_e32 v63, v69
	v_mov_b32_e32 v51, v69
	v_lshl_add_u64 v[110:111], s[82:83], 0, v[4:5]
	s_movk_i32 s90, 0x780
	s_mov_b32 s91, 0
	v_mov_b32_e32 v3, v2
	v_mov_b32_e32 v4, v2
	v_mov_b32_e32 v5, v2
	v_mov_b32_e32 v6, v2
	v_mov_b32_e32 v7, v2
	v_mov_b32_e32 v8, v2
	v_mov_b32_e32 v9, v2
	v_mov_b32_e32 v10, v2
	v_mov_b32_e32 v11, v2
	v_mov_b32_e32 v12, v2
	v_mov_b32_e32 v13, v2
	v_mov_b32_e32 v14, v2
	v_mov_b32_e32 v15, v2
	v_mov_b32_e32 v16, v2
	v_mov_b32_e32 v17, v2
	v_mov_b32_e32 v18, v2
	v_mov_b32_e32 v19, v2
	v_mov_b32_e32 v20, v2
	v_mov_b32_e32 v21, v2
	v_mov_b32_e32 v22, v2
	v_mov_b32_e32 v23, v2
	v_mov_b32_e32 v24, v2
	v_mov_b32_e32 v25, v2
	v_mov_b32_e32 v26, v2
	v_mov_b32_e32 v27, v2
	v_mov_b32_e32 v28, v2
	v_mov_b32_e32 v29, v2
	v_mov_b32_e32 v30, v2
	v_mov_b32_e32 v31, v2
	v_mov_b32_e32 v32, v2
	v_mov_b32_e32 v33, v2
	s_mov_b32 s92, 0xbfb8aa3b
	s_mov_b32 s93, 0xbfb8aa3b
	s_branch .LBB0_357

.LBB0_357:
	s_waitcnt vmcnt(27)
	v_lshlrev_b32_e32 v34, 16, v87
	v_and_b32_e32 v35, 0xffff0000, v87
	v_mul_f32_e32 v34, 0xbfb8aa3b, v34
	v_mul_f32_e32 v35, 0xbfb8aa3b, v35
	v_exp_f32_e32 v34, v34
	v_exp_f32_e32 v35, v35
	s_waitcnt vmcnt(24)
	v_lshlrev_b32_e32 v36, 16, v93
	v_add_u32_e32 v167, 0, v190
	v_add_f32_e32 v34, 1.0, v34
	v_add_f32_e32 v35, 1.0, v35
	v_rcp_f32_e32 v34, v34
	v_rcp_f32_e32 v35, v35
	s_andn2_b64 vcc, exec, s[74:75]
	s_mov_b64 s[58:59], -1
	v_pk_mul_f32 v[120:121], v[108:109], v[34:35]
	v_and_b32_e32 v34, 0xffff0000, v93
	v_mul_f32_e32 v35, 0xbfb8aa3b, v36
	v_mul_f32_e32 v34, 0xbfb8aa3b, v34
	v_exp_f32_e32 v35, v35
	v_exp_f32_e32 v36, v34
	v_add_f32_e32 v37, v64, v120
	v_add_f32_e32 v38, v65, v121
	v_add_f32_e32 v34, 1.0, v35
	v_add_f32_e32 v35, 1.0, v36
	v_rcp_f32_e32 v34, v34
	v_rcp_f32_e32 v35, v35
	v_log_f32_e32 v36, v37
	v_log_f32_e32 v37, v38
	v_pk_mul_f32 v[122:123], v[108:109], v[34:35]
	s_waitcnt vmcnt(19)
	v_lshlrev_b32_e32 v34, 16, v146
	v_and_b32_e32 v35, 0xffff0000, v146
	v_pk_mul_f32 v[34:35], v[34:35], s[92:93]
	v_exp_f32_e32 v34, v34
	v_exp_f32_e32 v35, v35
	v_pk_add_f32 v[38:39], v[64:65], v[122:123]
	v_pk_add_f32 v[34:35], v[34:35], 1.0 op_sel_hi:[1,0]
	v_rcp_f32_e32 v34, v34
	v_rcp_f32_e32 v35, v35
	v_log_f32_e32 v38, v38
	v_log_f32_e32 v39, v39
	v_pk_add_f32 v[144:145], v[36:37], 0 op_sel_hi:[1,0]
	v_pk_mul_f32 v[128:129], v[108:109], v[34:35]
	s_waitcnt vmcnt(18)
	v_lshlrev_b32_e32 v34, 16, v149
	v_and_b32_e32 v35, 0xffff0000, v149
	v_pk_mul_f32 v[34:35], v[34:35], s[92:93]
	v_exp_f32_e32 v34, v34
	v_exp_f32_e32 v35, v35
	v_pk_add_f32 v[40:41], v[64:65], v[128:129]
	v_pk_add_f32 v[34:35], v[34:35], 1.0 op_sel_hi:[1,0]
	v_rcp_f32_e32 v34, v34
	v_rcp_f32_e32 v35, v35
	v_log_f32_e32 v40, v40
	v_log_f32_e32 v41, v41
	v_pk_add_f32 v[140:141], v[144:145], v[38:39]
	v_pk_mul_f32 v[126:127], v[108:109], v[34:35]
	s_waitcnt vmcnt(15)
	v_lshlrev_b32_e32 v34, 16, v152
	v_and_b32_e32 v35, 0xffff0000, v152
	v_pk_mul_f32 v[34:35], v[34:35], s[92:93]
	v_exp_f32_e32 v34, v34
	v_exp_f32_e32 v35, v35
	v_pk_add_f32 v[42:43], v[64:65], v[126:127]
	v_pk_add_f32 v[34:35], v[34:35], 1.0 op_sel_hi:[1,0]
	v_rcp_f32_e32 v34, v34
	v_rcp_f32_e32 v35, v35
	v_log_f32_e32 v42, v42
	v_log_f32_e32 v43, v43
	v_pk_add_f32 v[136:137], v[140:141], v[40:41]
	v_pk_mul_f32 v[130:131], v[108:109], v[34:35]
	s_waitcnt vmcnt(11)
	v_lshlrev_b32_e32 v34, 16, v155
	v_and_b32_e32 v35, 0xffff0000, v155
	v_pk_mul_f32 v[34:35], v[34:35], s[92:93]
	v_exp_f32_e32 v34, v34
	v_exp_f32_e32 v35, v35
	v_pk_add_f32 v[44:45], v[64:65], v[130:131]
	v_pk_add_f32 v[34:35], v[34:35], 1.0 op_sel_hi:[1,0]
	v_rcp_f32_e32 v34, v34
	v_rcp_f32_e32 v35, v35
	v_log_f32_e32 v44, v44
	v_log_f32_e32 v45, v45
	v_pk_add_f32 v[132:133], v[136:137], v[42:43]
	v_pk_mul_f32 v[134:135], v[108:109], v[34:35]
	s_waitcnt vmcnt(9)
	v_lshlrev_b32_e32 v34, 16, v158
	v_and_b32_e32 v35, 0xffff0000, v158
	v_pk_mul_f32 v[34:35], v[34:35], s[92:93]
	v_exp_f32_e32 v34, v34
	v_exp_f32_e32 v35, v35
	v_pk_add_f32 v[46:47], v[64:65], v[134:135]
	v_pk_add_f32 v[34:35], v[34:35], 1.0 op_sel_hi:[1,0]
	v_rcp_f32_e32 v34, v34
	v_rcp_f32_e32 v35, v35
	v_log_f32_e32 v46, v46
	v_log_f32_e32 v47, v47
	v_pk_add_f32 v[124:125], v[132:133], v[44:45]
	v_pk_mul_f32 v[138:139], v[108:109], v[34:35]
	s_waitcnt vmcnt(6)
	v_lshlrev_b32_e32 v34, 16, v161
	v_and_b32_e32 v35, 0xffff0000, v161
	v_pk_mul_f32 v[34:35], v[34:35], s[92:93]
	v_exp_f32_e32 v34, v34
	v_exp_f32_e32 v35, v35
	v_pk_add_f32 v[48:49], v[64:65], v[138:139]
	v_pk_add_f32 v[34:35], v[34:35], 1.0 op_sel_hi:[1,0]
	v_rcp_f32_e32 v34, v34
	v_rcp_f32_e32 v35, v35
	v_log_f32_e32 v48, v48
	v_log_f32_e32 v49, v49
	v_pk_add_f32 v[118:119], v[124:125], v[46:47]
	v_pk_mul_f32 v[142:143], v[108:109], v[34:35]
	v_and_b32_e32 v36, 0xffff, v154
	v_pk_add_f32 v[34:35], v[64:65], v[142:143]
	v_log_f32_e32 v34, v34
	v_log_f32_e32 v35, v35
	v_pk_add_f32 v[114:115], v[118:119], v[48:49]
	v_and_b32_e32 v37, 0xffff, v160
	v_lshl_or_b32 v36, v157, 16, v36
	v_pk_add_f32 v[112:113], v[114:115], v[34:35]
	v_add_u32_e32 v34, s63, v190
	ds_write_b64 v34, v[112:113]
	v_and_b32_e32 v34, 0xffff, v91
	v_and_b32_e32 v35, 0xffff, v148
	v_lshl_or_b32 v34, v107, 16, v34
	v_lshl_or_b32 v35, v151, 16, v35
	s_waitcnt vmcnt(4)
	v_lshl_or_b32 v37, v165, 16, v37
	v_lshrrev_b32_e32 v38, 16, v91
	v_lshrrev_b32_e32 v39, 16, v148
	v_lshrrev_b32_e32 v40, 16, v154
	v_lshrrev_b32_e32 v41, 16, v160
	v_add_u32_e32 v42, s64, v191
	v_and_or_b32 v38, v107, s53, v38
	v_and_or_b32 v39, v151, s53, v39
	v_and_or_b32 v40, v157, s53, v40
	v_and_or_b32 v41, v165, s53, v41
	ds_write_b128 v42, v[34:37] offset:53248
	ds_write_b128 v42, v[38:41] offset:53392
	s_waitcnt lgkmcnt(0)
	s_barrier
	v_add_u32_e32 v34, 0x24c00, v167
	ds_read2st64_b64 v[46:49], v34 offset1:1
	ds_read2st64_b64 v[42:45], v34 offset0:2 offset1:3
	ds_read2st64_b64 v[38:41], v34 offset0:4 offset1:5
	ds_read2st64_b64 v[34:37], v34 offset0:6 offset1:7
	s_waitcnt lgkmcnt(3)
	v_add_f32_e32 v166, 0, v46
	v_add_f32_e32 v46, v166, v48
	s_waitcnt lgkmcnt(2)
	v_add_f32_e32 v46, v46, v42
	v_add_f32_e32 v46, v46, v44
	s_waitcnt lgkmcnt(1)
	v_add_f32_e32 v46, v46, v38
	v_add_f32_e32 v46, v46, v40
	s_waitcnt lgkmcnt(0)
	v_add_f32_e32 v46, v46, v34
	v_add_f32_e32 v46, v46, v36
	v_exp_f32_e32 v116, v46
	s_cbranch_vccnz .LBB0_359
	s_mov_b64 s[58:59], 0
